# mLSTM-out units: wave 0 gate and bias loads issued at the top of the unit with the operand rows; the vector step no longer waits for the state fragment loads
# baseline (speedup 1.0000x reference)
; #define LAS __attribute__((address_space(3)))
; DI void refresh(Frame& F) { int t_ = F.tid; asm volatile("" : "+v"(t_)); F.tid = t_; F.lane = t_ & 63; F.wave = __builtin_amdgcn_readfirstlane(t_ >> 6); size_t z_ = 0; unsigned zl_ = 0; asm volatile("" : "+s"(z_), "+s"(zl_)); F.ws = F.ws + z_; F.lds = F.lds + zl_; }
; DI void ml_out_load(Frame& F, int ch, int h, MlPre& P) {
;     const bf16* proj = (const bf16*)(F.ws + WS_PROJ); const size_t t0 = (size_t)ch * CHUNK;
; #pragma unroll
;     for (int j = 0; j < 2; ++j) { const int i = F.tid + 512 * j, r = i >> 3, c = (i & 7) * 8; const bf16* p = proj + (t0 + r) * PP + h * 64 + c;
;         P.q[j] = *(const v4u*)(p + O_LQ); P.k[j] = *(const v4u*)(p + O_LK); P.o[j] = *(const v4u*)(p + O_LO); }
;     { const int s = F.tid >> 2, cg = F.tid & 3; const bf16* vp = proj + (t0 + s) * PP + O_LV + h * 64 + cg * 16; P.v[0] = *(const v4u*)vp; P.v[1] = *(const v4u*)(vp + 8); }
; }
; template <class Hook = NoHook> DI void ml_out_unit(Frame& F, int l, int ch, int h, const MlPre& P, Hook mid = Hook()) {
;     refresh(F);
;     LAS bf16* QL = (LAS bf16*)F.lds;
;     LAS bf16* KL = QL + 128 * LP64;
;     LAS bf16* OL = KL + 128 * LP64;
;     LAS bf16* VT = OL + 128 * LP64;
;     LAS bf16* WL = VT + 80 * LP;
;     LAS float* A = (LAS float*)(F.lds + 3 * 128 * LP64 * 2 + (80 + 128) * LP * 2); LAS float* IG = A + 128; LAS float* E1 = IG + 128; LAS float* INTER = E1 + 128; LAS float* EMT = INTER + 128; LAS float* RED = EMT + 128;
;     const int t0 = ch * CHUNK; const bf16* proj = (const bf16*)(F.ws + WS_PROJ);
; #pragma unroll
;     for (int j = 0; j < 2; ++j) { const int i = F.tid + 512 * j, r = i >> 3, c = (i & 7) * 8;
;         *(LAS v4u*)(QL + r * LP64 + c) = P.q[j]; *(LAS v4u*)(KL + r * LP64 + c) = P.k[j]; *(LAS v4u*)(OL + r * LP64 + c) = P.o[j]; }
;     { const int s = F.tid >> 2, cg = F.tid & 3;
;       const v4u r0 = P.v[0], r1 = P.v[1];
; #pragma unroll
;       for (int e = 0; e < 4; ++e) { VT[(cg * 16 + 2 * e) * LP + s] = (bf16)(r0[e] & 0xffffu); VT[(cg * 16 + 2 * e + 1) * LP + s] = (bf16)(r0[e] >> 16);
;           VT[(cg * 16 + 8 + 2 * e) * LP + s] = (bf16)(r1[e] & 0xffffu); VT[(cg * 16 + 8 + 2 * e + 1) * LP + s] = (bf16)(r1[e] >> 16); } }
;     for (int i = F.tid; i < 16 * 128; i += 512) VT[(64 + (i >> 7)) * LP + (i & 127)] = (i < 128) ? (bf16)0x3f80u : (bf16)0;
.LBB0_2849:
	s_or_b64 exec, exec, s[0:1]
	v_mov_b32_e32 v0, s17
	s_waitcnt lgkmcnt(0)
	s_barrier
	ds_read_b32 v0, v0
	s_waitcnt lgkmcnt(0)
	s_barrier
	v_readfirstlane_b32 s0, v0
	s_cmpk_gt_i32 s0, 0x3ff
	s_cselect_b64 s[26:27], -1, 0
	s_and_b64 vcc, exec, s[26:27]
	s_cbranch_vccnz .LBB0_2901
	s_ashr_i32 s2, s0, 2
	s_and_b32 s29, s0, 3
	v_readfirstlane_b32 s1, v130
	s_cmp_gt_u32 s1, 63
	s_cbranch_scc1 .Lmy_mlo_skip
	s_add_i32 s1, s36, 0x20868
	v_mov_b32_e32 v162, s1
	ds_read2_b32 v[164:165], v162 offset1:1
	ds_read2_b32 v[166:167], v162 offset0:2 offset1:3
	s_lshl_b32 s3, s2, 7
	v_and_b32_e32 v163, 63, v130
	v_lshl_or_b32 v163, v163, 1, s3
	v_lshlrev_b32_e32 v163, 6, v163
	s_lshl_b32 s3, s29, 2
	v_add_u32_e32 v163, s3, v163
	s_add_u32 s4, s20, 0x500000
	s_addc_u32 s5, s21, 0
	global_load_dword v154, v163, s[4:5] offset:48
	global_load_dword v155, v163, s[4:5] offset:32
	global_load_dword v156, v163, s[4:5] offset:96
	global_load_dword v157, v163, s[4:5] offset:112
	s_or_b32 s3, s29, s22
	s_lshl_b32 s3, s3, 2
	s_waitcnt lgkmcnt(0)
	v_readfirstlane_b32 s6, v164
	v_readfirstlane_b32 s7, v165
	v_readfirstlane_b32 s8, v166
	v_readfirstlane_b32 s9, v167
	s_add_u32 s6, s6, s3
	s_addc_u32 s7, s7, 0
	s_add_u32 s8, s8, s3
	s_addc_u32 s9, s9, 0
	global_load_dword v159, v3, s[6:7]
	global_load_dword v158, v3, s[8:9]
.Lmy_mlo_skip:
	s_add_u32 s4, s20, 0xb100000
	s_addc_u32 s5, s21, 0
	s_ashr_i32 s3, s2, 31
	s_lshl_b64 s[6:7], s[2:3], 7
	s_lshl_b32 s52, s29, 7
	s_add_u32 s8, s4, s52
	v_ashrrev_i32_e32 v0, 3, v130
	s_addc_u32 s9, s5, 0
	v_ashrrev_i32_e32 v1, 31, v0
	v_lshl_add_u64 v[0:1], s[6:7], 0, v[0:1]
	v_mov_b64_e32 v[16:17], s[8:9]
	v_mad_u64_u32 v[4:5], s[8:9], v0, s33, v[16:17]
	v_lshlrev_b32_e32 v0, 4, v130
	v_mad_i32_i24 v5, v1, s33, v5
	v_and_b32_e32 v2, 0x70, v0
	v_lshl_add_u64 v[0:1], v[4:5], 0, v[2:3]
	v_add_co_u32_e32 v0, vcc, s64, v0
	v_mov_b64_e32 v[28:29], s[4:5]
	s_nop 0
	v_addc_co_u32_e32 v1, vcc, 0, v1, vcc
	global_load_dwordx4 v[4:7], v[0:1], off offset:512
	global_load_dwordx4 v[8:11], v[0:1], off offset:1024
	global_load_dwordx4 v[12:15], v[0:1], off offset:2048
	v_add_u32_e32 v0, 0x200, v130
	v_ashrrev_i32_e32 v0, 3, v0
	v_ashrrev_i32_e32 v1, 31, v0
	v_lshl_add_u64 v[0:1], s[6:7], 0, v[0:1]
	v_mad_u64_u32 v[16:17], s[8:9], v0, s33, v[16:17]
	v_mad_i32_i24 v17, v1, s33, v17
	v_lshl_add_u64 v[0:1], v[16:17], 0, v[2:3]
	v_add_co_u32_e32 v0, vcc, s64, v0
	v_lshlrev_b32_e32 v2, 5, v130
	s_nop 0
	v_addc_co_u32_e32 v1, vcc, 0, v1, vcc
	global_load_dwordx4 v[16:19], v[0:1], off offset:512
	global_load_dwordx4 v[20:23], v[0:1], off offset:1024
	global_load_dwordx4 v[24:27], v[0:1], off offset:2048
	v_ashrrev_i32_e32 v0, 2, v130
	v_ashrrev_i32_e32 v1, 31, v0
	v_lshl_add_u64 v[0:1], s[6:7], 0, v[0:1]
	v_mad_u64_u32 v[28:29], s[4:5], v0, s33, v[28:29]
	v_mad_i32_i24 v29, v1, s33, v29
	v_lshl_add_u64 v[0:1], v[28:29], 0, s[52:53]
	v_and_b32_e32 v2, 0x60, v2
	v_lshl_add_u64 v[0:1], v[0:1], 0, v[2:3]
	s_mov_b64 s[4:5], 0x1600
	v_lshl_add_u64 v[32:33], v[0:1], 0, s[4:5]
	v_add_co_u32_e32 v0, vcc, s64, v0
	s_mov_b64 s[4:5], 0
	s_nop 0
	v_addc_co_u32_e32 v1, vcc, 0, v1, vcc
	global_load_dwordx4 v[28:31], v[0:1], off offset:1536
	s_nop 0
	global_load_dwordx4 v[32:35], v[32:33], off offset:16
	s_mov_b32 s23, s53
	v_lshrrev_b32_e32 v0, 3, v130
	s_movk_i32 s1, 0x90
	v_lshlrev_b32_e32 v1, 4, v130
	s_add_i32 s51, s36, s23
	v_mul_lo_u32 v0, v0, s1
	v_and_b32_e32 v2, 0x70, v1
	v_add3_u32 v0, s51, v0, v2
	v_add_u32_e32 v131, 0x200, v130
	v_and_b32_e32 v1, 48, v1
	v_mul_u32_u24_e32 v1, 0x110, v1
	v_readfirstlane_b32 s34, v130
	v_cmp_gt_i32_e32 vcc, s67, v130
	s_waitcnt vmcnt(7)
	ds_write_b128 v0, v[4:7]
	s_waitcnt vmcnt(6)
	ds_write_b128 v0, v[8:11] offset:18432
	s_waitcnt vmcnt(5)
	ds_write_b128 v0, v[12:15] offset:36864
	v_lshrrev_b32_e32 v0, 3, v131
	v_mul_lo_u32 v0, v0, s1
	v_add3_u32 v0, s51, v0, v2
	s_waitcnt vmcnt(4)
	ds_write_b128 v0, v[16:19]
	s_waitcnt vmcnt(3)
	ds_write_b128 v0, v[20:23] offset:18432
	s_waitcnt vmcnt(2)
	ds_write_b128 v0, v[24:27] offset:36864
	v_ashrrev_i32_e32 v0, 2, v130
	v_lshlrev_b32_e32 v0, 1, v0
	v_add3_u32 v0, s51, v1, v0
	s_waitcnt vmcnt(1)
	ds_write_b16 v0, v28 offset:55296
	ds_write_b16_d16_hi v0, v28 offset:55568
	s_waitcnt vmcnt(0)
	ds_write_b16 v0, v32 offset:57472
	ds_write_b16_d16_hi v0, v32 offset:57744
	ds_write_b16 v0, v29 offset:55840
	ds_write_b16_d16_hi v0, v29 offset:56112
	ds_write_b16 v0, v33 offset:58016
	ds_write_b16_d16_hi v0, v33 offset:58288
	ds_write_b16 v0, v30 offset:56384
	ds_write_b16_d16_hi v0, v30 offset:56656
	ds_write_b16 v0, v34 offset:58560
	ds_write_b16_d16_hi v0, v34 offset:58832
	ds_write_b16 v0, v31 offset:56928
	ds_write_b16_d16_hi v0, v31 offset:57200
	ds_write_b16 v0, v35 offset:59104
	ds_write_b16_d16_hi v0, v35 offset:59376
	s_and_saveexec_b64 s[6:7], vcc
	s_cbranch_execz .LBB0_2858
	v_max_i32_e32 v0, 0x600, v130
	v_sub_u32_e32 v0, v0, v130
	v_add_u32_e32 v2, 0x1ff, v0
	v_and_b32_e32 v1, 0x7f, v130
	v_cmp_lt_u32_e32 vcc, s68, v2
	s_mov_b64 s[10:11], -1
	v_mov_b32_e32 v4, v130
	s_and_saveexec_b64 s[8:9], vcc
	s_cbranch_execz .LBB0_2855
	v_lshrrev_b32_e32 v0, 9, v2
	v_add_u32_e32 v2, 1, v0
	v_and_b32_e32 v8, 0xfffffc, v2
	v_add_u32_e32 v133, 0x600, v130
	v_add_u32_e32 v132, 0x400, v130
	v_mov_b64_e32 v[4:5], v[130:131]
	s_mov_b64 s[10:11], 0
	v_mov_b32_e32 v9, v8
	v_mov_b64_e32 v[6:7], v[132:133]
	s_movk_i32 s1, 0x7f
	s_mov_b32 s3, 0x11c00

; #define LAS __attribute__((address_space(3)))
; DI float log_sigmoid_f(float x) { return fminf(x, 0.f) - log1pf(__expf(-fabsf(x))); }
; DI void ml_vectors(Frame& F, int l, int t0, int h, LAS float* A, LAS float* IG, LAS float* RED) {
;     (void)RED;
;     if (F.wave == 0) {
;         const int s0 = 2 * F.lane; const float* gp = (const float*)(F.ws + WS_GATES) + (size_t)(t0 + s0) * 16; const float fb = inp(F, I_FB)[l * 4 + h], ib = inp(F, I_IB)[l * 4 + h];
;         float a0 = log_sigmoid_f(gp[12 + h] + fb), a1 = log_sigmoid_f(gp[16 + 12 + h] + fb);
;         IG[s0] = gp[8 + h] + ib; IG[s0 + 1] = gp[16 + 8 + h] + ib;
;         wscan2<false>(a0, a1, F.lane);
;         A[s0] = a0; A[s0 + 1] = a1; }
; template <class Hook = NoHook> DI void ml_out_unit(Frame& F, int l, int ch, int h, const MlPre& P, Hook mid = Hook()) {
;     ...
;     const bf16* cin = (const bf16*)(F.ws + WS_MLC + ML_ALT(F.l) * (406 * MiB)) + (size_t)(ch * 4 + h) * 5120;
;     bf16x8 cb[2][5];
; #pragma unroll
;     for (int ks = 0; ks < 2; ++ks)
; #pragma unroll
;         for (int nt = 0; nt < 5; ++nt) { cb[ks][nt] = *(const bf16x8*)(cin + (16 * nt + (F.lane & 15)) * 64 + 32 * ks + 8 * (F.lane >> 4)); if (nt == 4 && (F.lane & 15) != 0) cb[ks][nt] = (bf16x8){0, 0, 0, 0, 0, 0, 0, 0}; }
;     ml_vectors(F, l, t0, h, A, IG, RED);
.LBB0_2858:
	s_or_b64 exec, exec, s[6:7]
	s_add_u32 s20, s20, s4
	s_addc_u32 s21, s21, s5
	s_add_i32 s1, s51, 0x1b500
	s_add_i32 s35, s51, 0x1b700
	s_lshl_b32 s28, s2, 7
	s_mul_i32 s2, s0, 0x2800
	s_mul_hi_i32 s3, s0, 0x2800
	s_add_u32 s2, s20, s2
	s_addc_u32 s3, s21, s3
	v_and_b32_e32 v2, 48, v130
	v_lshlrev_b32_e32 v4, 7, v130
	v_and_b32_e32 v45, 63, v130
	v_lshl_add_u64 v[0:1], s[2:3], 0, v[2:3]
	s_mov_b64 s[2:3], 0x23500000
	v_and_b32_e32 v22, 0x780, v4
	v_lshl_add_u64 v[20:21], v[0:1], 0, s[2:3]
	v_mov_b32_e32 v23, v3
	v_or_b32_e32 v26, 0x1000, v22
	v_mov_b32_e32 v27, v3
	v_lshl_or_b32 v16, v45, 7, v235
	v_mov_b32_e32 v17, v3
	v_or_b32_e32 v42, 0x2000, v22
	v_mov_b32_e32 v43, v3
	s_mov_b64 s[2:3], 0x23500040
	v_lshl_add_u64 v[24:25], v[20:21], 0, v[22:23]
	v_lshl_add_u64 v[12:13], v[20:21], 0, v[26:27]
	v_lshl_add_u64 v[40:41], v[20:21], 0, v[16:17]
	v_lshl_add_u64 v[20:21], v[20:21], 0, v[42:43]
	v_lshl_add_u64 v[0:1], v[0:1], 0, s[2:3]
	global_load_dwordx4 v[8:11], v[24:25], off
	global_load_dwordx4 v[4:7], v[24:25], off offset:2048
	global_load_dwordx4 v[36:39], v[20:21], off
	v_lshl_add_u64 v[20:21], v[0:1], 0, v[26:27]
	global_load_dwordx4 v[12:15], v[12:13], off
	v_lshl_add_u64 v[0:1], v[0:1], 0, v[42:43]
	global_load_dwordx4 v[16:19], v[40:41], off
	global_load_dwordx4 v[28:31], v[24:25], off offset:64
	global_load_dwordx4 v[32:35], v[24:25], off offset:2112
	s_nop 0
	global_load_dwordx4 v[24:27], v[20:21], off
	s_nop 0
	global_load_dwordx4 v[20:23], v[40:41], off offset:64
	s_cmp_lt_u32 s34, 64
	global_load_dwordx4 v[40:43], v[0:1], off
	s_cselect_b64 s[30:31], -1, 0
	v_lshlrev_b32_e32 v50, 3, v45
	v_lshlrev_b32_e32 v1, 2, v45
	s_and_b64 vcc, exec, s[30:31]
	v_cmp_eq_u32_e64 s[2:3], 0, v45
	v_cmp_gt_u32_e64 s[12:13], 2, v45
	v_cmp_gt_u32_e64 s[10:11], 4, v45
	v_cmp_gt_u32_e64 s[8:9], 8, v45
	v_cmp_gt_u32_e64 s[6:7], 16, v45
	v_cmp_gt_u32_e64 s[4:5], 32, v45
	v_add_u32_e32 v51, s35, v50
	v_add_u32_e32 v57, 0xfc, v1
	v_add_u32_e32 v56, 0xf8, v1
	v_add_u32_e32 v55, 0xf0, v1
	v_add_u32_e32 v54, 0xe0, v1
	v_add_u32_e32 v53, 0xc0, v1
	v_xor_b32_e32 v52, 0x80, v1
	v_add_u32_e32 v58, s1, v50
	s_cbranch_vccz .LBB0_2860
	s_add_i32 s1, s51, 0x20870
	v_mov_b32_e32 v0, s1
	ds_read2_b32 v[48:49], v0 offset1:1
	s_or_b32 s38, s29, s22
	s_ashr_i32 s39, s38, 31
	s_lshl_b64 s[38:39], s[38:39], 2
	v_lshl_or_b32 v46, v45, 1, s28
	s_waitcnt lgkmcnt(0)
	v_readfirstlane_b32 s1, v48
	v_readfirstlane_b32 s37, v49
	s_add_u32 s40, s1, s38
	s_addc_u32 s41, s37, s39
	s_add_i32 s1, s51, 0x20868
	v_mov_b32_e32 v0, s1
	ds_read2_b32 v[60:61], v0 offset1:1
	v_ashrrev_i32_e32 v47, 31, v46
	v_lshlrev_b64 v[46:47], 6, v[46:47]
	v_lshl_add_u64 v[46:47], s[20:21], 0, v[46:47]
	v_mov_b32_e32 v48, v158
	s_waitcnt lgkmcnt(0)
	v_readfirstlane_b32 s1, v60
	v_readfirstlane_b32 s37, v61
	s_add_u32 s38, s1, s38
	s_addc_u32 s39, s37, s39
	s_lshl_b32 s52, s29, 2
	v_mov_b32_e32 v44, v159
	v_lshl_add_u64 v[46:47], v[46:47], 0, s[52:53]
	s_mov_b64 s[38:39], 0x500000
	v_lshl_add_u64 v[46:47], v[46:47], 0, s[38:39]
	v_mov_b32_e32 v0, v154
	v_mov_b32_e32 v152, v155
	v_mov_b32_e32 v153, v156
	v_mov_b32_e32 v151, v157
	s_waitcnt vmcnt(10)
	v_add_f32_e32 v0, v48, v0
	v_min_f32_e32 v49, 0, v0
	v_mul_f32_e64 v0, |v0|, s81
	v_exp_f32_e32 v0, v0
	s_nop 0
	v_add_f32_e32 v59, 1.0, v0
	v_add_f32_e32 v60, -1.0, v59
	v_sub_f32_e32 v61, v60, v59
	v_add_f32_e32 v61, 1.0, v61
	v_sub_f32_e32 v60, v0, v60
	v_add_f32_e32 v62, v60, v61
	v_frexp_mant_f32_e32 v60, v59
	v_cmp_gt_f32_e32 vcc, s87, v60
	v_cvt_f64_f32_e32 v[60:61], v59
	v_frexp_exp_i32_f64_e32 v60, v[60:61]
	v_subbrev_co_u32_e32 v60, vcc, 0, v60, vcc
	v_sub_u32_e32 v61, 0, v60
	v_ldexp_f32 v59, v59, v61
	v_ldexp_f32 v61, v62, v61
	v_add_f32_e32 v62, -1.0, v59
	v_add_f32_e32 v63, 1.0, v62
	v_sub_f32_e32 v63, v59, v63
	v_add_f32_e32 v63, v61, v63
	v_add_f32_e32 v64, v62, v63
	v_sub_f32_e32 v62, v64, v62
	v_sub_f32_e32 v62, v63, v62
	v_add_f32_e32 v63, 1.0, v59
	v_add_f32_e32 v65, -1.0, v63
	v_sub_f32_e32 v59, v59, v65
	v_add_f32_e32 v59, v61, v59
	v_add_f32_e32 v61, v63, v59
	v_sub_f32_e32 v63, v61, v63
	v_sub_f32_e32 v59, v59, v63
	v_rcp_f32_e32 v63, v61
	v_cvt_f32_i32_e32 v60, v60
	v_cmp_neq_f32_e32 vcc, s82, v0
	v_mul_f32_e32 v65, v64, v63
	v_mul_f32_e32 v66, v61, v65
	v_fma_f32 v67, v65, v61, -v66
	v_fmac_f32_e32 v67, v65, v59
	v_add_f32_e32 v68, v66, v67
	v_sub_f32_e32 v69, v64, v68
	v_sub_f32_e32 v64, v64, v69
	v_sub_f32_e32 v66, v68, v66
	v_sub_f32_e32 v64, v64, v68
	v_add_f32_e32 v62, v62, v64
	v_sub_f32_e32 v64, v66, v67
	v_add_f32_e32 v62, v64, v62
	v_add_f32_e32 v64, v69, v62
	v_mul_f32_e32 v66, v63, v64
	v_mul_f32_e32 v67, v61, v66
	v_fma_f32 v61, v66, v61, -v67
	v_fmac_f32_e32 v61, v66, v59
	v_sub_f32_e32 v59, v69, v64
	v_add_f32_e32 v59, v62, v59
	v_add_f32_e32 v62, v67, v61
	v_sub_f32_e32 v68, v64, v62
	v_sub_f32_e32 v64, v64, v68
	v_sub_f32_e32 v67, v62, v67
	v_sub_f32_e32 v62, v64, v62
	v_add_f32_e32 v59, v59, v62
	v_sub_f32_e32 v61, v67, v61
	v_add_f32_e32 v59, v61, v59
	v_add_f32_e32 v61, v65, v66
	v_add_f32_e32 v59, v68, v59
	v_sub_f32_e32 v62, v61, v65
	v_mul_f32_e32 v59, v63, v59
	v_sub_f32_e32 v62, v66, v62
	v_add_f32_e32 v59, v62, v59
	v_mul_f32_e32 v65, 0x3f317218, v60
	v_add_f32_e32 v62, v61, v59
	v_fma_f32 v66, v60, s80, -v65
	v_mul_f32_e32 v63, v62, v62
	v_fmac_f32_e32 v66, 0xb102e308, v60
	v_sub_f32_e32 v60, v62, v61
	v_fmamk_f32 v64, v63, 0x3e9b6dac, v216
	v_sub_f32_e32 v59, v59, v60
	v_add_f32_e32 v60, v65, v66
	v_fmaak_f32 v64, v63, v64, 0x3f2aaada
	v_sub_f32_e32 v61, v60, v65
	v_ldexp_f32 v65, v62, 1
	v_mul_f32_e32 v62, v62, v63
	v_mul_f32_e32 v62, v62, v64
	v_add_f32_e32 v63, v65, v62
	v_sub_f32_e32 v64, v63, v65
; #define LAS __attribute__((address_space(3)))
; DI float log_sigmoid_f(float x) { return fminf(x, 0.f) - log1pf(__expf(-fabsf(x))); }
; DI float shup(float v, int o, int lane) { return __int_as_float(__builtin_amdgcn_ds_bpermute(((lane - o) & 63) << 2, __float_as_int(v))); }
; template <bool IS_MAX> DI void wscan2(float& x0, float& x1, int lane) {
;     x1 = IS_MAX ? fmaxf(x0, x1) : x0 + x1;
;     float s = x1;
; #pragma unroll
;     for (int o = 1; o < 64; o <<= 1) { const float y = shup(s, o, lane); if (lane >= o) s = IS_MAX ? fmaxf(s, y) : s + y; }
;     const float ex = shup(s, 1, lane);
;     if (lane > 0) { x0 = IS_MAX ? fmaxf(x0, ex) : x0 + ex; x1 = IS_MAX ? fmaxf(x1, ex) : x1 + ex; }
; }
; DI void ml_vectors(Frame& F, int l, int t0, int h, LAS float* A, LAS float* IG, LAS float* RED) {
;     (void)RED;
;     if (F.wave == 0) {
;         const int s0 = 2 * F.lane; const float* gp = (const float*)(F.ws + WS_GATES) + (size_t)(t0 + s0) * 16; const float fb = inp(F, I_FB)[l * 4 + h], ib = inp(F, I_IB)[l * 4 + h];
;         float a0 = log_sigmoid_f(gp[12 + h] + fb), a1 = log_sigmoid_f(gp[16 + 12 + h] + fb);
;         IG[s0] = gp[8 + h] + ib; IG[s0 + 1] = gp[16 + 8 + h] + ib;
;         wscan2<false>(a0, a1, F.lane);
;         A[s0] = a0; A[s0 + 1] = a1; }
;     __syncthreads();
; }
	v_ldexp_f32 v59, v59, 1
	v_sub_f32_e32 v62, v62, v64
	v_add_f32_e32 v59, v59, v62
	v_add_f32_e32 v62, v63, v59
	v_sub_f32_e32 v63, v62, v63
	v_sub_f32_e32 v59, v59, v63
	v_add_f32_e32 v63, v60, v62
	v_sub_f32_e32 v64, v63, v60
	v_sub_f32_e32 v65, v63, v64
	v_sub_f32_e32 v61, v66, v61
	v_sub_f32_e32 v60, v60, v65
	v_sub_f32_e32 v62, v62, v64
	v_add_f32_e32 v60, v62, v60
	v_add_f32_e32 v62, v61, v59
	v_sub_f32_e32 v64, v62, v61
	v_sub_f32_e32 v65, v62, v64
	v_sub_f32_e32 v61, v61, v65
	v_sub_f32_e32 v59, v59, v64
	v_add_f32_e32 v60, v62, v60
	v_add_f32_e32 v59, v59, v61
	v_add_f32_e32 v61, v63, v60
	v_sub_f32_e32 v62, v61, v63
	v_sub_f32_e32 v60, v60, v62
	v_add_f32_e32 v59, v59, v60
	v_add_f32_e32 v59, v61, v59
	v_cndmask_b32_e32 v59, v230, v59, vcc
	v_cmp_ngt_f32_e32 vcc, -1.0, v0
	s_nop 1
	v_cndmask_b32_e32 v59, v231, v59, vcc
	v_cmp_neq_f32_e32 vcc, -1.0, v0
	s_nop 1
	v_cndmask_b32_e32 v59, v232, v59, vcc
	v_cmp_lt_f32_e64 vcc, |v0|, s86
	s_nop 1
	v_cndmask_b32_e32 v0, v59, v0, vcc
	v_sub_f32_e32 v59, v49, v0
	v_add_f32_e32 v0, v48, v151
	v_min_f32_e32 v60, 0, v0
	v_mul_f32_e64 v0, |v0|, s81
	v_exp_f32_e32 v0, v0
	s_nop 0
	v_add_f32_e32 v61, 1.0, v0
	v_add_f32_e32 v48, -1.0, v61
	v_sub_f32_e32 v49, v48, v61
	v_add_f32_e32 v49, 1.0, v49
	v_sub_f32_e32 v48, v0, v48
	v_add_f32_e32 v62, v48, v49
	v_frexp_mant_f32_e32 v48, v61
	v_cmp_gt_f32_e32 vcc, s87, v48
	v_cvt_f64_f32_e32 v[48:49], v61
	v_frexp_exp_i32_f64_e32 v48, v[48:49]
	v_subbrev_co_u32_e32 v48, vcc, 0, v48, vcc
	v_sub_u32_e32 v49, 0, v48
	v_ldexp_f32 v61, v61, v49
	v_ldexp_f32 v49, v62, v49
	v_add_f32_e32 v62, -1.0, v61
	v_add_f32_e32 v63, 1.0, v62
	v_sub_f32_e32 v63, v61, v63
	v_add_f32_e32 v63, v49, v63
	v_add_f32_e32 v64, v62, v63
	v_sub_f32_e32 v62, v64, v62
	v_sub_f32_e32 v62, v63, v62
	v_add_f32_e32 v63, 1.0, v61
	v_add_f32_e32 v65, -1.0, v63
	v_sub_f32_e32 v61, v61, v65
	v_add_f32_e32 v49, v49, v61
	v_add_f32_e32 v61, v63, v49
	v_sub_f32_e32 v63, v61, v63
	v_sub_f32_e32 v49, v49, v63
	v_rcp_f32_e32 v63, v61
	v_cvt_f32_i32_e32 v48, v48
	v_cmp_neq_f32_e32 vcc, s82, v0
	v_mul_f32_e32 v65, v64, v63
	v_mul_f32_e32 v66, v61, v65
	v_fma_f32 v67, v65, v61, -v66
	v_fmac_f32_e32 v67, v65, v49
	v_add_f32_e32 v68, v66, v67
	v_sub_f32_e32 v69, v64, v68
	v_sub_f32_e32 v64, v64, v69
	v_sub_f32_e32 v66, v68, v66
	v_sub_f32_e32 v64, v64, v68
	v_add_f32_e32 v62, v62, v64
	v_sub_f32_e32 v64, v66, v67
	v_add_f32_e32 v62, v64, v62
	v_add_f32_e32 v64, v69, v62
	v_mul_f32_e32 v66, v63, v64
	v_mul_f32_e32 v67, v61, v66
	v_fma_f32 v61, v66, v61, -v67
	v_fmac_f32_e32 v61, v66, v49
	v_sub_f32_e32 v49, v69, v64
	v_add_f32_e32 v49, v62, v49
	v_add_f32_e32 v62, v67, v61
	v_sub_f32_e32 v68, v64, v62
	v_sub_f32_e32 v64, v64, v68
	v_sub_f32_e32 v67, v62, v67
	v_sub_f32_e32 v62, v64, v62
	v_add_f32_e32 v49, v49, v62
	v_sub_f32_e32 v61, v67, v61
	v_add_f32_e32 v49, v61, v49
	v_add_f32_e32 v61, v65, v66
	v_add_f32_e32 v49, v68, v49
	v_sub_f32_e32 v62, v61, v65
	v_mul_f32_e32 v49, v63, v49
	v_sub_f32_e32 v62, v66, v62
	v_add_f32_e32 v49, v62, v49
	v_mul_f32_e32 v65, 0x3f317218, v48
	v_add_f32_e32 v62, v61, v49
	v_fma_f32 v66, v48, s80, -v65
	v_mul_f32_e32 v63, v62, v62
	v_fmac_f32_e32 v66, 0xb102e308, v48
	v_sub_f32_e32 v48, v62, v61
	v_fmamk_f32 v64, v63, 0x3e9b6dac, v216
	v_sub_f32_e32 v48, v49, v48
	v_add_f32_e32 v49, v65, v66
	v_fmaak_f32 v64, v63, v64, 0x3f2aaada
	v_sub_f32_e32 v61, v49, v65
	v_ldexp_f32 v65, v62, 1
	v_mul_f32_e32 v62, v62, v63
	v_mul_f32_e32 v62, v62, v64
	v_add_f32_e32 v63, v65, v62
	v_sub_f32_e32 v64, v63, v65
	v_ldexp_f32 v48, v48, 1
	v_sub_f32_e32 v62, v62, v64
	v_add_f32_e32 v48, v48, v62
	v_add_f32_e32 v62, v63, v48
	v_sub_f32_e32 v63, v62, v63
	v_sub_f32_e32 v48, v48, v63
	v_add_f32_e32 v63, v49, v62
	v_sub_f32_e32 v64, v63, v49
	v_sub_f32_e32 v65, v63, v64
	v_sub_f32_e32 v61, v66, v61
	v_sub_f32_e32 v49, v49, v65
	v_sub_f32_e32 v62, v62, v64
	v_add_f32_e32 v49, v62, v49
	v_add_f32_e32 v62, v61, v48
	v_sub_f32_e32 v64, v62, v61
	v_sub_f32_e32 v65, v62, v64
	v_sub_f32_e32 v61, v61, v65
	v_sub_f32_e32 v48, v48, v64
	v_add_f32_e32 v49, v62, v49
	v_add_f32_e32 v48, v48, v61
	v_add_f32_e32 v61, v63, v49
	v_sub_f32_e32 v62, v61, v63
	v_sub_f32_e32 v49, v49, v62
	v_add_f32_e32 v48, v48, v49
	v_add_f32_e32 v48, v61, v48
	v_cndmask_b32_e32 v48, v230, v48, vcc
	v_cmp_ngt_f32_e32 vcc, -1.0, v0
	s_nop 1
	v_cndmask_b32_e32 v48, v231, v48, vcc
	v_cmp_neq_f32_e32 vcc, -1.0, v0
	s_nop 1
	v_cndmask_b32_e32 v48, v232, v48, vcc
	v_cmp_lt_f32_e64 vcc, |v0|, s86
	s_nop 1
	v_cndmask_b32_e32 v0, v48, v0, vcc
	v_mov_b32_e32 v48, v152
	v_mov_b32_e32 v49, v153
	v_sub_f32_e32 v60, v60, v0
	v_add_f32_e32 v0, v59, v60
	s_nop 0
	v_pk_add_f32 v[46:47], v[44:45], v[48:49] op_sel_hi:[0,1]
	v_and_b32_e32 v44, 0xfc, v57
	ds_write2_b32 v51, v46, v47 offset1:1
	ds_bpermute_b32 v46, v44, v0
	v_and_b32_e32 v47, 0xfc, v56
	s_waitcnt lgkmcnt(0)
	v_add_f32_e32 v46, v0, v46
	v_cndmask_b32_e64 v46, v46, v0, s[2:3]
	ds_bpermute_b32 v47, v47, v46
	s_waitcnt lgkmcnt(0)
	v_add_f32_e32 v47, v46, v47
	v_cndmask_b32_e64 v46, v47, v46, s[12:13]
	v_and_b32_e32 v47, 0xfc, v55
	ds_bpermute_b32 v47, v47, v46
	s_waitcnt lgkmcnt(0)
	v_add_f32_e32 v47, v46, v47
	v_cndmask_b32_e64 v46, v47, v46, s[10:11]
	v_and_b32_e32 v47, 0xfc, v54
	ds_bpermute_b32 v47, v47, v46
	s_waitcnt lgkmcnt(0)
	v_add_f32_e32 v47, v46, v47
	v_cndmask_b32_e64 v46, v47, v46, s[8:9]
	v_and_b32_e32 v47, 0xfc, v53
	ds_bpermute_b32 v47, v47, v46
	s_waitcnt lgkmcnt(0)
	v_add_f32_e32 v47, v46, v47
	v_cndmask_b32_e64 v46, v47, v46, s[6:7]
	ds_bpermute_b32 v47, v52, v46
	s_waitcnt lgkmcnt(0)
	v_add_f32_e32 v47, v46, v47
	v_cndmask_b32_e64 v46, v47, v46, s[4:5]
	ds_bpermute_b32 v44, v44, v46
	s_waitcnt lgkmcnt(0)
	v_add_f32_e32 v46, v59, v44
	v_add_f32_e32 v44, v0, v44
	v_cndmask_b32_e64 v46, v46, v59, s[2:3]
	v_cndmask_b32_e64 v0, v44, v0, s[2:3]
	ds_write2_b32 v58, v46, v0 offset1:1
